# speedup vs baseline: 1.0006x; 1.0006x over previous
.LBB1_20:
	v_exp_f32_e32 v16, v16
	s_lshl_b32 s15, s13, 4
	v_exp_f32_e32 v17, v17
	s_add_i32 s15, s10, s15
	v_exp_f32_e32 v18, v18
	v_mov_b32_e32 v91, s15
	v_mov_b32_e32 v92, s14
	v_exp_f32_e32 v19, v19
	v_lshl_add_u32 v226, s13, 14, v89
	ds_write_b32 v91, v92
	v_add_f32_e32 v91, 0, v16
	v_exp_f32_e32 v20, v20
	v_add_f32_e32 v91, v91, v17
	v_exp_f32_e32 v21, v21
	v_add_f32_e32 v91, v91, v18
	v_exp_f32_e32 v22, v22
	v_add_f32_e32 v91, v91, v19
	v_exp_f32_e32 v23, v23
	v_add_f32_e32 v91, v91, v20
	v_exp_f32_e32 v24, v24
	v_add_f32_e32 v91, v91, v21
	v_exp_f32_e32 v25, v25
	v_add_f32_e32 v91, v91, v22
	v_exp_f32_e32 v26, v26
	v_add_f32_e32 v91, v91, v23
	v_cvt_pk_bf16_f32 v16, v16, v17
	v_cvt_pk_bf16_f32 v17, v18, v19
	v_cvt_pk_bf16_f32 v18, v20, v21
	v_cvt_pk_bf16_f32 v19, v22, v23
	ds_write_b128 v226, v[16:19]
	v_exp_f32_e32 v27, v27
	v_add_f32_e32 v91, v91, v24
	v_exp_f32_e32 v28, v28
	v_add_f32_e32 v91, v91, v25
	v_exp_f32_e32 v29, v29
	v_add_f32_e32 v91, v91, v26
	v_exp_f32_e32 v30, v30
	v_add_f32_e32 v91, v91, v27
	v_exp_f32_e32 v31, v31
	v_add_f32_e32 v91, v91, v28
	v_exp_f32_e32 v32, v32
	v_add_f32_e32 v91, v91, v29
	v_exp_f32_e32 v33, v33
	v_add_f32_e32 v91, v91, v30
	v_exp_f32_e32 v34, v34
	v_add_f32_e32 v91, v91, v31
	v_cvt_pk_bf16_f32 v16, v24, v25
	v_cvt_pk_bf16_f32 v17, v26, v27
	v_cvt_pk_bf16_f32 v18, v28, v29
	v_cvt_pk_bf16_f32 v19, v30, v31
	ds_write_b128 v226, v[16:19] offset:1024
	v_exp_f32_e32 v35, v35
	v_add_f32_e32 v91, v91, v32
	v_exp_f32_e32 v36, v36
	v_add_f32_e32 v91, v91, v33
	v_exp_f32_e32 v37, v37
	v_add_f32_e32 v91, v91, v34
	v_exp_f32_e32 v38, v38
	v_add_f32_e32 v91, v91, v35
	v_exp_f32_e32 v39, v39
	v_add_f32_e32 v91, v91, v36
	v_exp_f32_e32 v40, v40
	v_add_f32_e32 v91, v91, v37
	v_exp_f32_e32 v41, v41
	v_add_f32_e32 v91, v91, v38
	v_exp_f32_e32 v42, v42
	v_add_f32_e32 v91, v91, v39
	v_cvt_pk_bf16_f32 v16, v32, v33
	v_cvt_pk_bf16_f32 v17, v34, v35
	v_cvt_pk_bf16_f32 v18, v36, v37
	v_cvt_pk_bf16_f32 v19, v38, v39
	ds_write_b128 v226, v[16:19] offset:2048
	v_exp_f32_e32 v43, v43
	v_add_f32_e32 v91, v91, v40
	v_exp_f32_e32 v44, v44
	v_add_f32_e32 v91, v91, v41
	v_exp_f32_e32 v45, v45
	v_add_f32_e32 v91, v91, v42
	v_exp_f32_e32 v46, v46
	v_add_f32_e32 v91, v91, v43
	v_exp_f32_e32 v47, v47
	v_add_f32_e32 v91, v91, v44
	v_add_f32_e32 v91, v91, v45
	v_add_f32_e32 v91, v91, v46
	v_add_f32_e32 v91, v91, v47
	v_cvt_pk_bf16_f32 v16, v40, v41
	v_cvt_pk_bf16_f32 v17, v42, v43
	v_cvt_pk_bf16_f32 v18, v44, v45
	v_cvt_pk_bf16_f32 v19, v46, v47
	ds_write_b128 v226, v[16:19] offset:3072
	v_add_f32_e32 v99, v99, v91
	s_add_i32 s13, s5, 0x8000
	s_cmp_lg_u32 s5, 0x10000
	s_cselect_b32 s5, s13, 0
	s_add_i32 s11, s11, 1
	s_cmp_eq_u32 s11, 16
	s_waitcnt lgkmcnt(0)
	s_barrier
	s_cbranch_scc1 .LBB1_23
